# final plus non-temporal stores for the prologue weight transposes (bf16/fp8 converted mixer weights)
# baseline (speedup 1.0000x reference)
; template <bool F8> DI void item_gather(const TItem& d, LAS float* scr, int lane) {
;     if constexpr (F8) {
;         const int nl = lane >> 2, kc = lane & 3;
;         unsigned char* base = d.WT + (size_t)d.drow0 * d.Kd + d.kofs + d.k0;
;         unsigned voff = (unsigned)(nl * d.Kd + 16 * kc); asm volatile("" : "+v"(voff));
;         f32x4 x[16];
; #pragma unroll
;         for (int t = 0; t < 4; ++t) { const int n = nl + 16 * t; const int sw = 4 * (((n >> 2) & 15) ^ (n & 3));
; #pragma unroll
;             for (int q = 0; q < 4; ++q) { const int kq = 16 * kc + 4 * q; x[t * 4 + q] = *(const LAS f32x4*)(scr + n * 64 + (kq ^ sw)); } }
;         asm volatile("s_waitcnt lgkmcnt(0)" : "+v"(x[0]), "+v"(x[1]), "+v"(x[2]), "+v"(x[3]), "+v"(x[4]), "+v"(x[5]), "+v"(x[6]), "+v"(x[7]),
;                      "+v"(x[8]), "+v"(x[9]), "+v"(x[10]), "+v"(x[11]), "+v"(x[12]), "+v"(x[13]), "+v"(x[14]), "+v"(x[15]) :: "memory");
; #pragma unroll
;         for (int t = 0; t < 4; ++t) { u32x4 o;
; #pragma unroll
;             for (int q = 0; q < 4; ++q) { const f32x4 y = x[t * 4 + q]; o[q] = pk4_fp8(y[0] * W8_SCALE, y[1] * W8_SCALE, y[2] * W8_SCALE, y[3] * W8_SCALE); }
;             *(u32x4*)(base + (size_t)t * 16 * d.Kd + voff) = o; }
;     } else {
;         const int nl = lane >> 3, kc = lane & 7;
;         unsigned char* base = d.WT + ((size_t)d.drow0 * d.Kd + d.kofs + d.k0) * 2;
;         unsigned voff = (unsigned)(nl * d.Kd + 8 * kc) * 2u; asm volatile("" : "+v"(voff));
;         f32x4 x[16];
; #pragma unroll
;         for (int t = 0; t < 8; ++t) { const int n = nl + 8 * t; const int sw = 4 * (((n >> 2) & 15) ^ (n & 3));
; #pragma unroll
;             for (int q = 0; q < 2; ++q) { const int kq = 8 * kc + 4 * q; x[t * 2 + q] = *(const LAS f32x4*)(scr + n * 64 + (kq ^ sw)); } }
;         asm volatile("s_waitcnt lgkmcnt(0)" : "+v"(x[0]), "+v"(x[1]), "+v"(x[2]), "+v"(x[3]), "+v"(x[4]), "+v"(x[5]), "+v"(x[6]), "+v"(x[7]),
;                      "+v"(x[8]), "+v"(x[9]), "+v"(x[10]), "+v"(x[11]), "+v"(x[12]), "+v"(x[13]), "+v"(x[14]), "+v"(x[15]) :: "memory");
; #pragma unroll
;         for (int t = 0; t < 8; ++t) { u32x4 o;
; #pragma unroll
;             for (int q = 0; q < 2; ++q) { const f32x4 y = x[t * 2 + q]; o[2 * q] = pk2(y[0], y[1]); o[2 * q + 1] = pk2(y[2], y[3]); }
;             *(u32x4*)(base + (size_t)t * 8 * d.Kd * 2 + voff) = o; }
;     }
.LBB0_119:
	s_ashr_i32 s22, s33, 31
	s_mul_hi_u32 s25, s8, s33
	s_mul_i32 s22, s8, s22
	s_add_i32 s25, s25, s22
	s_mul_i32 s26, s8, s33
	s_ashr_i32 s24, s35, 31
	s_mov_b64 s[22:23], -1
	s_and_b64 vcc, exec, s[20:21]
	s_cbranch_vccz .LBB0_121
	v_mul_lo_u32 v64, s8, v136
	v_add_lshl_u32 v68, v64, v137, 1
	s_add_u32 s20, s12, s35
	ds_read_b128 v[64:67], v154
	ds_read_b128 v[174:177], v153
	ds_read_b128 v[178:181], v152
	ds_read_b128 v[182:185], v151
	ds_read_b128 v[186:189], v150
	ds_read_b128 v[190:193], v149
	ds_read_b128 v[194:197], v148
	ds_read_b128 v[198:201], v147
	ds_read_b128 v[202:205], v145
	ds_read_b128 v[206:209], v144
	ds_read_b128 v[210:213], v143
	ds_read_b128 v[214:217], v142
	ds_read_b128 v[218:221], v141
	ds_read_b128 v[222:225], v140
	ds_read_b128 v[226:229], v139
	ds_read_b128 v[230:233], v138
	s_addc_u32 s21, s13, s24
	s_add_u32 s20, s20, s26
	s_addc_u32 s21, s21, s25
	s_lshl_b64 s[20:21], s[20:21], 1
	s_add_u32 s20, s10, s20
	s_waitcnt lgkmcnt(0)
	s_waitcnt lgkmcnt(0)
	s_addc_u32 s21, s11, s21
	v_cvt_pk_bf16_f32 v230, v230, v231
	v_cvt_pk_bf16_f32 v231, v232, v233
	v_cvt_pk_bf16_f32 v232, v226, v227
	v_cvt_pk_bf16_f32 v233, v228, v229
	v_lshl_add_u64 v[234:235], s[20:21], 0, v[68:69]
	global_store_dwordx4 v68, v[230:233], s[20:21] nt
	s_lshl_b64 s[20:21], s[8:9], 4
	v_cvt_pk_bf16_f32 v222, v222, v223
	v_cvt_pk_bf16_f32 v223, v224, v225
	v_cvt_pk_bf16_f32 v224, v218, v219
	v_lshl_add_u64 v[218:219], v[234:235], 0, s[20:21]
	v_cvt_pk_bf16_f32 v214, v214, v215
	v_cvt_pk_bf16_f32 v215, v216, v217
	v_cvt_pk_bf16_f32 v216, v210, v211
	v_lshl_add_u64 v[210:211], v[218:219], 0, s[20:21]
	v_cvt_pk_bf16_f32 v206, v206, v207
	v_cvt_pk_bf16_f32 v207, v208, v209
	v_cvt_pk_bf16_f32 v208, v202, v203
	v_lshl_add_u64 v[202:203], v[210:211], 0, s[20:21]
	v_cvt_pk_bf16_f32 v198, v198, v199
	v_cvt_pk_bf16_f32 v199, v200, v201
	v_cvt_pk_bf16_f32 v200, v194, v195
	v_lshl_add_u64 v[194:195], v[202:203], 0, s[20:21]
	v_cvt_pk_bf16_f32 v190, v190, v191
	v_cvt_pk_bf16_f32 v191, v192, v193
	v_cvt_pk_bf16_f32 v192, v186, v187
	v_lshl_add_u64 v[186:187], v[194:195], 0, s[20:21]
	v_cvt_pk_bf16_f32 v182, v182, v183
	v_cvt_pk_bf16_f32 v183, v184, v185
	v_cvt_pk_bf16_f32 v184, v178, v179
	v_lshl_add_u64 v[178:179], v[186:187], 0, s[20:21]
	v_cvt_pk_bf16_f32 v225, v220, v221
	v_cvt_pk_bf16_f32 v217, v212, v213
	v_cvt_pk_bf16_f32 v209, v204, v205
	v_cvt_pk_bf16_f32 v201, v196, v197
	v_cvt_pk_bf16_f32 v193, v188, v189
	v_cvt_pk_bf16_f32 v185, v180, v181
	v_cvt_pk_bf16_f32 v174, v174, v175
	v_cvt_pk_bf16_f32 v175, v176, v177
	v_cvt_pk_bf16_f32 v176, v64, v65
	v_cvt_pk_bf16_f32 v177, v66, v67
	v_lshl_add_u64 v[64:65], v[178:179], 0, s[20:21]
	global_store_dwordx4 v[218:219], v[222:225], off nt
	global_store_dwordx4 v[210:211], v[214:217], off nt
	global_store_dwordx4 v[202:203], v[206:209], off nt
	global_store_dwordx4 v[194:195], v[198:201], off nt
	global_store_dwordx4 v[186:187], v[190:193], off nt
	global_store_dwordx4 v[178:179], v[182:185], off nt
	global_store_dwordx4 v[64:65], v[174:177], off nt
	s_waitcnt lgkmcnt(0)
	s_mov_b64 s[22:23], 0
.LBB0_121:
	s_andn2_b64 vcc, exec, s[22:23]
	s_cbranch_vccnz .LBB0_94
	v_mad_u64_u32 v[234:235], s[20:21], s8, v155, v[70:71]
	ds_read_b128 v[64:67], v171
	ds_read_b128 v[174:177], v170
	ds_read_b128 v[178:181], v169
	ds_read_b128 v[182:185], v168
	ds_read_b128 v[186:189], v167
	ds_read_b128 v[190:193], v166
	ds_read_b128 v[194:197], v165
	ds_read_b128 v[198:201], v164
	ds_read_b128 v[202:205], v163
	ds_read_b128 v[206:209], v162
	ds_read_b128 v[210:213], v161
	ds_read_b128 v[214:217], v160
	ds_read_b128 v[218:221], v159
	ds_read_b128 v[222:225], v158
	ds_read_b128 v[226:229], v157
	ds_read_b128 v[230:233], v156
	s_add_u32 s10, s10, s26
	s_addc_u32 s11, s11, s25
	s_waitcnt lgkmcnt(0)
	s_waitcnt lgkmcnt(0)
; #define LAS __attribute__((address_space(3)))
; DI unsigned pk4_fp8(float a, float b, float c, float d) { int r = 0; r = __builtin_amdgcn_cvt_pk_fp8_f32(sat8(a), sat8(b), r, false); r = __builtin_amdgcn_cvt_pk_fp8_f32(sat8(c), sat8(d), r, true); return (unsigned)r; }
; template <bool F8> DI void item_gather(const TItem& d, LAS float* scr, int lane) {
;     if constexpr (F8) {
;         const int nl = lane >> 2, kc = lane & 3;
;         unsigned char* base = d.WT + (size_t)d.drow0 * d.Kd + d.kofs + d.k0;
;         unsigned voff = (unsigned)(nl * d.Kd + 16 * kc); asm volatile("" : "+v"(voff));
;         f32x4 x[16];
; #pragma unroll
;         for (int t = 0; t < 4; ++t) { const int n = nl + 16 * t; const int sw = 4 * (((n >> 2) & 15) ^ (n & 3));
; #pragma unroll
;             for (int q = 0; q < 4; ++q) { const int kq = 16 * kc + 4 * q; x[t * 4 + q] = *(const LAS f32x4*)(scr + n * 64 + (kq ^ sw)); } }
;         asm volatile("s_waitcnt lgkmcnt(0)" : "+v"(x[0]), "+v"(x[1]), "+v"(x[2]), "+v"(x[3]), "+v"(x[4]), "+v"(x[5]), "+v"(x[6]), "+v"(x[7]),
;                      "+v"(x[8]), "+v"(x[9]), "+v"(x[10]), "+v"(x[11]), "+v"(x[12]), "+v"(x[13]), "+v"(x[14]), "+v"(x[15]) :: "memory");
; #pragma unroll
;         for (int t = 0; t < 4; ++t) { u32x4 o;
; #pragma unroll
;             for (int q = 0; q < 4; ++q) { const f32x4 y = x[t * 4 + q]; o[q] = pk4_fp8(y[0] * W8_SCALE, y[1] * W8_SCALE, y[2] * W8_SCALE, y[3] * W8_SCALE); }
;             *(u32x4*)(base + (size_t)t * 16 * d.Kd + voff) = o; }
;     } else {
	s_nop 0
	v_mul_f32_e32 v68, 0x42800000, v230
	v_mul_f32_e32 v173, 0x42800000, v231
	v_med3_f32 v68, v68, s34, v172
	v_med3_f32 v173, v173, s34, v172
	v_mov_b32_e32 v230, v69
	v_cvt_pk_fp8_f32 v230, v68, v173
	v_mul_f32_e32 v231, 0x42800000, v232
	v_mul_f32_e32 v68, 0x42800000, v233
	v_med3_f32 v173, v231, s34, v172
	v_med3_f32 v68, v68, s34, v172
	v_cvt_pk_fp8_f32 v230, v173, v68 op_sel:[0,0,1]
	v_mul_f32_e32 v68, 0x42800000, v226
	v_mul_f32_e32 v173, 0x42800000, v227
	v_med3_f32 v68, v68, s34, v172
	v_med3_f32 v173, v173, s34, v172
	v_mov_b32_e32 v231, v69
	v_cvt_pk_fp8_f32 v231, v68, v173
	v_mul_f32_e32 v226, 0x42800000, v228
	v_mul_f32_e32 v68, 0x42800000, v229
	v_med3_f32 v173, v226, s34, v172
	v_med3_f32 v68, v68, s34, v172
	v_cvt_pk_fp8_f32 v231, v173, v68 op_sel:[0,0,1]
	v_mul_f32_e32 v68, 0x42800000, v222
	v_mul_f32_e32 v173, 0x42800000, v223
	v_med3_f32 v68, v68, s34, v172
	v_med3_f32 v173, v173, s34, v172
	v_mov_b32_e32 v232, v69
	v_cvt_pk_fp8_f32 v232, v68, v173
	v_mul_f32_e32 v222, 0x42800000, v224
	v_mul_f32_e32 v68, 0x42800000, v225
	v_med3_f32 v173, v222, s34, v172
	v_med3_f32 v68, v68, s34, v172
	v_cvt_pk_fp8_f32 v232, v173, v68 op_sel:[0,0,1]
	v_mul_f32_e32 v68, 0x42800000, v218
	v_mul_f32_e32 v173, 0x42800000, v219
	v_med3_f32 v68, v68, s34, v172
	v_med3_f32 v173, v173, s34, v172
	v_mov_b32_e32 v233, v69
	v_cvt_pk_fp8_f32 v233, v68, v173
	v_mul_f32_e32 v218, 0x42800000, v220
	v_mul_f32_e32 v68, 0x42800000, v221
	v_med3_f32 v173, v218, s34, v172
	v_med3_f32 v68, v68, s34, v172
	v_cvt_pk_fp8_f32 v233, v173, v68 op_sel:[0,0,1]
	v_mul_f32_e32 v68, 0x42800000, v214
	v_mul_f32_e32 v173, 0x42800000, v215
	v_med3_f32 v68, v68, s34, v172
	v_med3_f32 v173, v173, s34, v172
	v_mov_b32_e32 v214, v69
	v_cvt_pk_fp8_f32 v214, v68, v173
	v_mul_f32_e32 v215, 0x42800000, v216
	v_mul_f32_e32 v68, 0x42800000, v217
	v_med3_f32 v173, v215, s34, v172
	v_med3_f32 v68, v68, s34, v172
	v_cvt_pk_fp8_f32 v214, v173, v68 op_sel:[0,0,1]
	v_mul_f32_e32 v68, 0x42800000, v210
	v_mul_f32_e32 v173, 0x42800000, v211
	v_med3_f32 v68, v68, s34, v172
	v_med3_f32 v173, v173, s34, v172
	v_mov_b32_e32 v215, v69
	v_cvt_pk_fp8_f32 v215, v68, v173
	v_mul_f32_e32 v210, 0x42800000, v212
	v_mul_f32_e32 v68, 0x42800000, v213
	v_med3_f32 v173, v210, s34, v172
	v_med3_f32 v68, v68, s34, v172
	v_cvt_pk_fp8_f32 v215, v173, v68 op_sel:[0,0,1]
	v_mul_f32_e32 v68, 0x42800000, v206
	v_mul_f32_e32 v173, 0x42800000, v207
	v_med3_f32 v68, v68, s34, v172
	v_med3_f32 v173, v173, s34, v172
	v_mov_b32_e32 v216, v69
	v_cvt_pk_fp8_f32 v216, v68, v173
	v_mul_f32_e32 v206, 0x42800000, v208
	v_mul_f32_e32 v68, 0x42800000, v209
	v_med3_f32 v173, v206, s34, v172
	v_med3_f32 v68, v68, s34, v172
	v_cvt_pk_fp8_f32 v216, v173, v68 op_sel:[0,0,1]
	v_mul_f32_e32 v68, 0x42800000, v202
	v_mul_f32_e32 v173, 0x42800000, v203
	v_med3_f32 v68, v68, s34, v172
	v_med3_f32 v173, v173, s34, v172
	v_mov_b32_e32 v217, v69
	v_cvt_pk_fp8_f32 v217, v68, v173
	v_mul_f32_e32 v202, 0x42800000, v204
	v_mul_f32_e32 v68, 0x42800000, v205
	v_med3_f32 v173, v202, s34, v172
	v_med3_f32 v68, v68, s34, v172
	v_cvt_pk_fp8_f32 v217, v173, v68 op_sel:[0,0,1]
	v_mul_f32_e32 v68, 0x42800000, v198
	v_mul_f32_e32 v173, 0x42800000, v199
	v_med3_f32 v68, v68, s34, v172
	v_med3_f32 v173, v173, s34, v172
	v_mov_b32_e32 v198, v69
	v_cvt_pk_fp8_f32 v198, v68, v173
	v_mul_f32_e32 v199, 0x42800000, v200
	v_mul_f32_e32 v68, 0x42800000, v201
	v_med3_f32 v173, v199, s34, v172
	v_med3_f32 v68, v68, s34, v172
	v_cvt_pk_fp8_f32 v198, v173, v68 op_sel:[0,0,1]
	v_mul_f32_e32 v68, 0x42800000, v194
	v_mul_f32_e32 v173, 0x42800000, v195
	v_med3_f32 v68, v68, s34, v172
	v_med3_f32 v173, v173, s34, v172
	v_mov_b32_e32 v199, v69
	v_cvt_pk_fp8_f32 v199, v68, v173
	v_mul_f32_e32 v194, 0x42800000, v196
	v_mul_f32_e32 v68, 0x42800000, v197
	v_med3_f32 v173, v194, s34, v172
	v_med3_f32 v68, v68, s34, v172
	v_cvt_pk_fp8_f32 v199, v173, v68 op_sel:[0,0,1]
	v_mul_f32_e32 v68, 0x42800000, v190
	v_mul_f32_e32 v173, 0x42800000, v191
	v_med3_f32 v68, v68, s34, v172
	v_med3_f32 v173, v173, s34, v172
	v_mov_b32_e32 v200, v69
	v_cvt_pk_fp8_f32 v200, v68, v173
	v_mul_f32_e32 v190, 0x42800000, v192
	v_mul_f32_e32 v68, 0x42800000, v193
	v_med3_f32 v173, v190, s34, v172
	v_med3_f32 v68, v68, s34, v172
	v_cvt_pk_fp8_f32 v200, v173, v68 op_sel:[0,0,1]
	v_mul_f32_e32 v68, 0x42800000, v186
	v_mul_f32_e32 v173, 0x42800000, v187
	v_med3_f32 v68, v68, s34, v172
	v_med3_f32 v173, v173, s34, v172
	v_mov_b32_e32 v201, v69
	v_cvt_pk_fp8_f32 v201, v68, v173
	v_mul_f32_e32 v186, 0x42800000, v188
	v_mul_f32_e32 v68, 0x42800000, v189
	v_med3_f32 v173, v186, s34, v172
	v_med3_f32 v68, v68, s34, v172
	v_cvt_pk_fp8_f32 v201, v173, v68 op_sel:[0,0,1]
	v_mul_f32_e32 v68, 0x42800000, v182
	v_mul_f32_e32 v173, 0x42800000, v183
	v_med3_f32 v68, v68, s34, v172
	v_med3_f32 v173, v173, s34, v172
	v_mov_b32_e32 v182, v69
	v_cvt_pk_fp8_f32 v182, v68, v173
	v_mul_f32_e32 v183, 0x42800000, v184
	v_mul_f32_e32 v68, 0x42800000, v185
	v_med3_f32 v173, v183, s34, v172
	v_med3_f32 v68, v68, s34, v172
	v_cvt_pk_fp8_f32 v182, v173, v68 op_sel:[0,0,1]
	v_mul_f32_e32 v68, 0x42800000, v178
	v_mul_f32_e32 v173, 0x42800000, v179
	v_med3_f32 v68, v68, s34, v172
	v_med3_f32 v173, v173, s34, v172
	v_mov_b32_e32 v183, v69
	v_cvt_pk_fp8_f32 v183, v68, v173
	v_mul_f32_e32 v178, 0x42800000, v180
	v_mul_f32_e32 v68, 0x42800000, v181
	v_med3_f32 v173, v178, s34, v172
	v_med3_f32 v68, v68, s34, v172
	v_cvt_pk_fp8_f32 v183, v173, v68 op_sel:[0,0,1]
	v_mul_f32_e32 v68, 0x42800000, v174
	v_mul_f32_e32 v173, 0x42800000, v175
	v_mul_f32_e32 v64, 0x42800000, v64
	v_mul_f32_e32 v65, 0x42800000, v65
	v_med3_f32 v68, v68, s34, v172
	v_med3_f32 v173, v173, s34, v172
	v_mov_b32_e32 v184, v69
	v_med3_f32 v64, v64, s34, v172
	v_med3_f32 v65, v65, s34, v172
	v_mov_b32_e32 v185, v69
	s_add_u32 s10, s10, s12
	v_cvt_pk_fp8_f32 v184, v68, v173
	v_cvt_pk_fp8_f32 v185, v64, v65
	s_addc_u32 s11, s11, s13
	s_add_u32 s10, s10, s35
	v_mul_f32_e32 v174, 0x42800000, v176
	v_mul_f32_e32 v68, 0x42800000, v177
	v_mul_f32_e32 v66, 0x42800000, v66
	v_mul_f32_e32 v64, 0x42800000, v67
	s_addc_u32 s11, s11, s24
	v_mov_b32_e32 v235, v69
	v_med3_f32 v173, v174, s34, v172
	v_med3_f32 v68, v68, s34, v172
	v_med3_f32 v65, v66, s34, v172
	v_med3_f32 v64, v64, s34, v172
	v_lshl_add_u64 v[236:237], s[10:11], 0, v[234:235]
	global_store_dwordx4 v234, v[230:233], s[10:11] nt
	s_lshl_b64 s[10:11], s[8:9], 4
	v_cvt_pk_fp8_f32 v184, v173, v68 op_sel:[0,0,1]
	v_cvt_pk_fp8_f32 v185, v65, v64 op_sel:[0,0,1]
	v_lshl_add_u64 v[202:203], v[236:237], 0, s[10:11]
	v_lshl_add_u64 v[64:65], v[202:203], 0, s[10:11]
	global_store_dwordx4 v[202:203], v[214:217], off nt
	global_store_dwordx4 v[64:65], v[198:201], off nt
	v_lshl_add_u64 v[64:65], v[64:65], 0, s[10:11]
	global_store_dwordx4 v[64:65], v[182:185], off nt
	s_waitcnt lgkmcnt(0)
	s_branch .LBB0_94
